# E33: E29 + MoE-down GEMM epilogue loads its column bias once per unit (was reloaded per row group, 3 serialized round trips per group -> 2)
# baseline (speedup 1.0000x reference)
.LBB0_1713:
	s_lshl_b32 s7, s30, 2
	s_add_i32 s7, s7, 0
	s_add_i32 s7, s7, 0x22700
	v_mov_b32_e32 v142, s7
	ds_read_b32 v142, v142
	s_lshl_b32 s7, s52, 2
	s_add_i32 s7, s7, 0
	s_add_i32 s7, s7, 0x22c00
	s_waitcnt lgkmcnt(0)
	v_readfirstlane_b32 s25, v142
	v_mov_b32_e32 v142, s7
	ds_read_b32 v142, v142
	v_add_u32_e32 v147, s25, v131
	s_waitcnt lgkmcnt(0)
	v_readfirstlane_b32 s7, v142
	s_nop 1
	v_cmp_gt_i32_e32 vcc, s7, v147
	v_lshl_or_b32 v142, s6, 8, v145
	s_add_i32 s34, s52, s50
	s_ashr_i32 s35, s34, 31
	s_lshl_b64 s[34:35], s[34:35], 12
	s_add_u32 s34, s44, s34
	v_ashrrev_i32_e32 v143, 31, v142
	s_addc_u32 s35, s16, s35
	v_lshl_add_u64 v[162:163], v[142:143], 2, s[34:35]
	global_load_dwordx4 v[164:167], v[162:163], off
	global_load_dwordx4 v[168:171], v[162:163], off offset:16
	global_load_dwordx4 v[172:175], v[162:163], off offset:512
	global_load_dwordx4 v[176:179], v[162:163], off offset:528
	s_and_saveexec_b64 s[30:31], vcc
	s_cbranch_execz .LBB0_1715
	v_lshl_add_u32 v148, s52, 14, v147
	v_ashrrev_i32_e32 v149, 31, v148
	v_lshl_add_u64 v[148:149], v[148:149], 2, s[12:13]
	global_load_dword v156, v[148:149], off
	s_add_i32 s34, s52, s50
	s_ashr_i32 s35, s34, 31
	s_lshl_b64 s[34:35], s[34:35], 12
	s_add_u32 s34, s44, s34
	v_ashrrev_i32_e32 v143, 31, v142
	s_addc_u32 s35, s16, s35
	v_lshl_add_u64 v[158:159], v[142:143], 2, s[34:35]
	s_waitcnt vmcnt(0)
	v_ashrrev_i32_e32 v157, 31, v156
	v_lshl_add_u64 v[160:161], v[156:157], 2, s[14:15]
	global_load_dword v160, v[160:161], off
	v_lshlrev_b64 v[156:157], 11, v[156:157]
	v_lshl_add_u64 v[156:157], s[10:11], 0, v[156:157]
	v_pk_add_f32 v[128:129], v[128:129], v[166:167]
	v_pk_add_f32 v[124:125], v[124:125], v[170:171]
	v_pk_add_f32 v[122:123], v[122:123], v[168:169]
	v_pk_add_f32 v[126:127], v[126:127], v[164:165]
	v_lshl_add_u64 v[148:149], v[142:143], 1, v[156:157]
	s_waitcnt vmcnt(0)
	v_pk_mul_f32 v[150:151], v[160:161], v[124:125] op_sel_hi:[0,1]
	v_pk_mul_f32 v[124:125], v[160:161], v[122:123] op_sel_hi:[0,1]
	v_pk_mul_f32 v[128:129], v[160:161], v[128:129] op_sel_hi:[0,1]
	v_pk_mul_f32 v[126:127], v[160:161], v[126:127] op_sel_hi:[0,1]
	v_cvt_pk_bf16_f32 v122, v126, v127
	v_cvt_pk_bf16_f32 v123, v128, v129
	v_cvt_pk_bf16_f32 v124, v124, v125
	v_cvt_pk_bf16_f32 v125, v150, v151
	global_store_dwordx4 v[148:149], v[122:125], off
	v_pk_add_f32 v[120:121], v[120:121], v[174:175]
	v_pk_add_f32 v[116:117], v[116:117], v[178:179]
	v_pk_add_f32 v[114:115], v[114:115], v[176:177]
	v_pk_add_f32 v[118:119], v[118:119], v[172:173]
	v_pk_mul_f32 v[122:123], v[160:161], v[116:117] op_sel_hi:[0,1]
	v_pk_mul_f32 v[116:117], v[160:161], v[114:115] op_sel_hi:[0,1]
	v_pk_mul_f32 v[120:121], v[160:161], v[120:121] op_sel_hi:[0,1]
	v_pk_mul_f32 v[118:119], v[160:161], v[118:119] op_sel_hi:[0,1]
	v_cvt_pk_bf16_f32 v114, v118, v119
	v_cvt_pk_bf16_f32 v115, v120, v121
	v_cvt_pk_bf16_f32 v116, v116, v117
	v_cvt_pk_bf16_f32 v117, v122, v123
	global_store_dwordx4 v[148:149], v[114:117], off offset:256
.LBB0_1715:
	s_or_b64 exec, exec, s[30:31]
	s_nop 0
	v_add_u32_e32 v114, 16, v147
	v_cmp_gt_i32_e32 vcc, s7, v114
	s_and_saveexec_b64 s[30:31], vcc
	s_cbranch_execz .LBB0_1717
	v_lshl_add_u32 v114, s52, 14, v114
	v_ashrrev_i32_e32 v115, 31, v114
	v_lshl_add_u64 v[114:115], v[114:115], 2, s[12:13]
	global_load_dword v122, v[114:115], off
	s_add_i32 s34, s52, s50
	s_ashr_i32 s35, s34, 31
	s_lshl_b64 s[34:35], s[34:35], 12
	s_add_u32 s34, s44, s34
	v_ashrrev_i32_e32 v143, 31, v142
	s_addc_u32 s35, s16, s35
	v_lshl_add_u64 v[124:125], v[142:143], 2, s[34:35]
	s_waitcnt vmcnt(0)
	v_ashrrev_i32_e32 v123, 31, v122
	v_lshl_add_u64 v[126:127], v[122:123], 2, s[14:15]
	global_load_dword v126, v[126:127], off
	v_lshlrev_b64 v[122:123], 11, v[122:123]
	v_lshl_add_u64 v[122:123], s[10:11], 0, v[122:123]
	v_pk_add_f32 v[112:113], v[112:113], v[166:167]
	v_pk_add_f32 v[108:109], v[108:109], v[170:171]
	v_pk_add_f32 v[106:107], v[106:107], v[168:169]
	v_pk_add_f32 v[110:111], v[110:111], v[164:165]
	v_lshl_add_u64 v[114:115], v[142:143], 1, v[122:123]
	s_waitcnt vmcnt(0)
	v_pk_mul_f32 v[116:117], v[126:127], v[108:109] op_sel_hi:[0,1]
	v_pk_mul_f32 v[108:109], v[126:127], v[106:107] op_sel_hi:[0,1]
	v_pk_mul_f32 v[112:113], v[126:127], v[112:113] op_sel_hi:[0,1]
	v_pk_mul_f32 v[110:111], v[126:127], v[110:111] op_sel_hi:[0,1]
	v_cvt_pk_bf16_f32 v106, v110, v111
	v_cvt_pk_bf16_f32 v107, v112, v113
	v_cvt_pk_bf16_f32 v108, v108, v109
	v_cvt_pk_bf16_f32 v109, v116, v117
	global_store_dwordx4 v[114:115], v[106:109], off
	v_pk_add_f32 v[104:105], v[104:105], v[174:175]
	v_pk_add_f32 v[98:99], v[98:99], v[178:179]
	v_pk_add_f32 v[96:97], v[96:97], v[176:177]
	v_pk_add_f32 v[102:103], v[102:103], v[172:173]
	v_pk_mul_f32 v[106:107], v[126:127], v[98:99] op_sel_hi:[0,1]
	v_pk_mul_f32 v[98:99], v[126:127], v[96:97] op_sel_hi:[0,1]
	v_pk_mul_f32 v[104:105], v[126:127], v[104:105] op_sel_hi:[0,1]
	v_pk_mul_f32 v[102:103], v[126:127], v[102:103] op_sel_hi:[0,1]
	v_cvt_pk_bf16_f32 v96, v102, v103
	v_cvt_pk_bf16_f32 v97, v104, v105
	v_cvt_pk_bf16_f32 v98, v98, v99
	v_cvt_pk_bf16_f32 v99, v106, v107
	global_store_dwordx4 v[114:115], v[96:99], off offset:256
.LBB0_1717:
	s_or_b64 exec, exec, s[30:31]
	s_nop 0
	v_add_u32_e32 v96, 32, v147
	v_cmp_gt_i32_e32 vcc, s7, v96
	s_and_saveexec_b64 s[30:31], vcc
	s_cbranch_execz .LBB0_1719
	v_lshl_add_u32 v96, s52, 14, v96
	v_ashrrev_i32_e32 v97, 31, v96
	v_lshl_add_u64 v[96:97], v[96:97], 2, s[12:13]
	global_load_dword v106, v[96:97], off
	s_add_i32 s34, s52, s50
	s_ashr_i32 s35, s34, 31
	s_lshl_b64 s[34:35], s[34:35], 12
	s_add_u32 s34, s44, s34
	v_ashrrev_i32_e32 v143, 31, v142
	s_addc_u32 s35, s16, s35
	v_lshl_add_u64 v[108:109], v[142:143], 2, s[34:35]
	s_waitcnt vmcnt(0)
	v_ashrrev_i32_e32 v107, 31, v106
	v_lshl_add_u64 v[110:111], v[106:107], 2, s[14:15]
	global_load_dword v110, v[110:111], off
	v_lshlrev_b64 v[106:107], 11, v[106:107]
	v_lshl_add_u64 v[106:107], s[10:11], 0, v[106:107]
	v_pk_add_f32 v[94:95], v[94:95], v[166:167]
	v_pk_add_f32 v[90:91], v[90:91], v[170:171]
	v_pk_add_f32 v[88:89], v[88:89], v[168:169]
	v_pk_add_f32 v[92:93], v[92:93], v[164:165]
	v_lshl_add_u64 v[96:97], v[142:143], 1, v[106:107]
	s_waitcnt vmcnt(0)
	v_pk_mul_f32 v[98:99], v[110:111], v[90:91] op_sel_hi:[0,1]
	v_pk_mul_f32 v[90:91], v[110:111], v[88:89] op_sel_hi:[0,1]
	v_pk_mul_f32 v[94:95], v[110:111], v[94:95] op_sel_hi:[0,1]
	v_pk_mul_f32 v[92:93], v[110:111], v[92:93] op_sel_hi:[0,1]
	v_cvt_pk_bf16_f32 v88, v92, v93
	v_cvt_pk_bf16_f32 v89, v94, v95
	v_cvt_pk_bf16_f32 v90, v90, v91
	v_cvt_pk_bf16_f32 v91, v98, v99
	global_store_dwordx4 v[96:97], v[88:91], off
	v_pk_add_f32 v[86:87], v[86:87], v[174:175]
	v_pk_add_f32 v[82:83], v[82:83], v[178:179]
	v_pk_add_f32 v[80:81], v[80:81], v[176:177]
	v_pk_add_f32 v[84:85], v[84:85], v[172:173]
	v_pk_mul_f32 v[88:89], v[110:111], v[82:83] op_sel_hi:[0,1]
	v_pk_mul_f32 v[82:83], v[110:111], v[80:81] op_sel_hi:[0,1]
	v_pk_mul_f32 v[86:87], v[110:111], v[86:87] op_sel_hi:[0,1]
	v_pk_mul_f32 v[84:85], v[110:111], v[84:85] op_sel_hi:[0,1]
	v_cvt_pk_bf16_f32 v80, v84, v85
	v_cvt_pk_bf16_f32 v81, v86, v87
	v_cvt_pk_bf16_f32 v82, v82, v83
	v_cvt_pk_bf16_f32 v83, v88, v89
	global_store_dwordx4 v[96:97], v[80:83], off offset:256
.LBB0_1719:
	s_or_b64 exec, exec, s[30:31]
	s_nop 0
	v_add_u32_e32 v80, 48, v147
	v_cmp_gt_i32_e32 vcc, s7, v80
	s_and_saveexec_b64 s[30:31], vcc
	s_cbranch_execz .LBB0_1721
	v_lshl_add_u32 v80, s52, 14, v80
	v_ashrrev_i32_e32 v81, 31, v80
	v_lshl_add_u64 v[80:81], v[80:81], 2, s[12:13]
	global_load_dword v88, v[80:81], off
	s_add_i32 s34, s52, s50
	s_ashr_i32 s35, s34, 31
	s_lshl_b64 s[34:35], s[34:35], 12
	s_add_u32 s34, s44, s34
	v_ashrrev_i32_e32 v143, 31, v142
	s_addc_u32 s35, s16, s35
	v_lshl_add_u64 v[90:91], v[142:143], 2, s[34:35]
	s_waitcnt vmcnt(0)
	v_ashrrev_i32_e32 v89, 31, v88
	v_lshl_add_u64 v[92:93], v[88:89], 2, s[14:15]
	global_load_dword v92, v[92:93], off
	v_lshlrev_b64 v[88:89], 11, v[88:89]
	v_lshl_add_u64 v[88:89], s[10:11], 0, v[88:89]
	v_pk_add_f32 v[78:79], v[78:79], v[166:167]
	v_pk_add_f32 v[74:75], v[74:75], v[170:171]
	v_pk_add_f32 v[72:73], v[72:73], v[168:169]
	v_pk_add_f32 v[76:77], v[76:77], v[164:165]
	v_lshl_add_u64 v[80:81], v[142:143], 1, v[88:89]
	s_waitcnt vmcnt(0)
	v_pk_mul_f32 v[82:83], v[92:93], v[74:75] op_sel_hi:[0,1]
	v_pk_mul_f32 v[74:75], v[92:93], v[72:73] op_sel_hi:[0,1]
	v_pk_mul_f32 v[78:79], v[92:93], v[78:79] op_sel_hi:[0,1]
	v_pk_mul_f32 v[76:77], v[92:93], v[76:77] op_sel_hi:[0,1]
	v_cvt_pk_bf16_f32 v72, v76, v77
	v_cvt_pk_bf16_f32 v73, v78, v79
	v_cvt_pk_bf16_f32 v74, v74, v75
	v_cvt_pk_bf16_f32 v75, v82, v83
	global_store_dwordx4 v[80:81], v[72:75], off
	v_pk_add_f32 v[70:71], v[70:71], v[174:175]
	v_pk_add_f32 v[66:67], v[66:67], v[178:179]
	v_pk_add_f32 v[64:65], v[64:65], v[176:177]
	v_pk_add_f32 v[68:69], v[68:69], v[172:173]
	v_pk_mul_f32 v[72:73], v[92:93], v[66:67] op_sel_hi:[0,1]
	v_pk_mul_f32 v[66:67], v[92:93], v[64:65] op_sel_hi:[0,1]
	v_pk_mul_f32 v[70:71], v[92:93], v[70:71] op_sel_hi:[0,1]
	v_pk_mul_f32 v[68:69], v[92:93], v[68:69] op_sel_hi:[0,1]
	v_cvt_pk_bf16_f32 v64, v68, v69
	v_cvt_pk_bf16_f32 v65, v70, v71
	v_cvt_pk_bf16_f32 v66, v66, v67
	v_cvt_pk_bf16_f32 v67, v72, v73
	global_store_dwordx4 v[80:81], v[64:67], off offset:256
.LBB0_1721:
	s_or_b64 exec, exec, s[30:31]
	s_nop 0
	v_add_u32_e32 v64, 0x80, v147
	v_cmp_gt_i32_e32 vcc, s7, v64
	s_and_saveexec_b64 s[30:31], vcc
	s_cbranch_execz .LBB0_1723
	v_lshl_add_u32 v64, s52, 14, v64
	v_ashrrev_i32_e32 v65, 31, v64
	v_lshl_add_u64 v[64:65], v[64:65], 2, s[12:13]
	global_load_dword v72, v[64:65], off
	s_add_i32 s34, s52, s50
	s_ashr_i32 s35, s34, 31
	s_lshl_b64 s[34:35], s[34:35], 12
	s_add_u32 s34, s44, s34
	v_ashrrev_i32_e32 v143, 31, v142
	s_addc_u32 s35, s16, s35
	v_lshl_add_u64 v[74:75], v[142:143], 2, s[34:35]
	s_waitcnt vmcnt(0)
	v_ashrrev_i32_e32 v73, 31, v72
	v_lshl_add_u64 v[76:77], v[72:73], 2, s[14:15]
	global_load_dword v76, v[76:77], off
	v_lshlrev_b64 v[72:73], 11, v[72:73]
	v_lshl_add_u64 v[72:73], s[10:11], 0, v[72:73]
	v_pk_add_f32 v[62:63], v[62:63], v[166:167]
	v_pk_add_f32 v[58:59], v[58:59], v[170:171]
	v_pk_add_f32 v[56:57], v[56:57], v[168:169]
	v_pk_add_f32 v[60:61], v[60:61], v[164:165]
	v_lshl_add_u64 v[64:65], v[142:143], 1, v[72:73]
	s_waitcnt vmcnt(0)
	v_pk_mul_f32 v[66:67], v[76:77], v[58:59] op_sel_hi:[0,1]
	v_pk_mul_f32 v[58:59], v[76:77], v[56:57] op_sel_hi:[0,1]
	v_pk_mul_f32 v[62:63], v[76:77], v[62:63] op_sel_hi:[0,1]
	v_pk_mul_f32 v[60:61], v[76:77], v[60:61] op_sel_hi:[0,1]
	v_cvt_pk_bf16_f32 v56, v60, v61
	v_cvt_pk_bf16_f32 v57, v62, v63
	v_cvt_pk_bf16_f32 v58, v58, v59
	v_cvt_pk_bf16_f32 v59, v66, v67
	global_store_dwordx4 v[64:65], v[56:59], off
	v_pk_add_f32 v[54:55], v[54:55], v[174:175]
	v_pk_add_f32 v[50:51], v[50:51], v[178:179]
	v_pk_add_f32 v[48:49], v[48:49], v[176:177]
	v_pk_add_f32 v[52:53], v[52:53], v[172:173]
	v_pk_mul_f32 v[56:57], v[76:77], v[50:51] op_sel_hi:[0,1]
	v_pk_mul_f32 v[50:51], v[76:77], v[48:49] op_sel_hi:[0,1]
	v_pk_mul_f32 v[54:55], v[76:77], v[54:55] op_sel_hi:[0,1]
	v_pk_mul_f32 v[52:53], v[76:77], v[52:53] op_sel_hi:[0,1]
	v_cvt_pk_bf16_f32 v48, v52, v53
	v_cvt_pk_bf16_f32 v49, v54, v55
	v_cvt_pk_bf16_f32 v50, v50, v51
	v_cvt_pk_bf16_f32 v51, v56, v57
	global_store_dwordx4 v[64:65], v[48:51], off offset:256
.LBB0_1723:
	s_or_b64 exec, exec, s[30:31]
	s_nop 0
	v_add_u32_e32 v48, 0x90, v147
	v_cmp_gt_i32_e32 vcc, s7, v48
	s_and_saveexec_b64 s[30:31], vcc
	s_cbranch_execz .LBB0_1725
	v_lshl_add_u32 v48, s52, 14, v48
	v_ashrrev_i32_e32 v49, 31, v48
	v_lshl_add_u64 v[48:49], v[48:49], 2, s[12:13]
	global_load_dword v56, v[48:49], off
	s_add_i32 s34, s52, s50
	s_ashr_i32 s35, s34, 31
	s_lshl_b64 s[34:35], s[34:35], 12
	s_add_u32 s34, s44, s34
	v_ashrrev_i32_e32 v143, 31, v142
	s_addc_u32 s35, s16, s35
	v_lshl_add_u64 v[58:59], v[142:143], 2, s[34:35]
	s_waitcnt vmcnt(0)
	v_ashrrev_i32_e32 v57, 31, v56
	v_lshl_add_u64 v[60:61], v[56:57], 2, s[14:15]
	global_load_dword v60, v[60:61], off
	v_lshlrev_b64 v[56:57], 11, v[56:57]
	v_lshl_add_u64 v[56:57], s[10:11], 0, v[56:57]
	v_pk_add_f32 v[46:47], v[46:47], v[166:167]
	v_pk_add_f32 v[42:43], v[42:43], v[170:171]
	v_pk_add_f32 v[40:41], v[40:41], v[168:169]
	v_pk_add_f32 v[44:45], v[44:45], v[164:165]
	v_lshl_add_u64 v[48:49], v[142:143], 1, v[56:57]
	s_waitcnt vmcnt(0)
	v_pk_mul_f32 v[50:51], v[60:61], v[42:43] op_sel_hi:[0,1]
	v_pk_mul_f32 v[42:43], v[60:61], v[40:41] op_sel_hi:[0,1]
	v_pk_mul_f32 v[46:47], v[60:61], v[46:47] op_sel_hi:[0,1]
	v_pk_mul_f32 v[44:45], v[60:61], v[44:45] op_sel_hi:[0,1]
	v_cvt_pk_bf16_f32 v40, v44, v45
	v_cvt_pk_bf16_f32 v41, v46, v47
	v_cvt_pk_bf16_f32 v42, v42, v43
	v_cvt_pk_bf16_f32 v43, v50, v51
	global_store_dwordx4 v[48:49], v[40:43], off
	v_pk_add_f32 v[38:39], v[38:39], v[174:175]
	v_pk_add_f32 v[34:35], v[34:35], v[178:179]
	v_pk_add_f32 v[32:33], v[32:33], v[176:177]
	v_pk_add_f32 v[36:37], v[36:37], v[172:173]
	v_pk_mul_f32 v[40:41], v[60:61], v[34:35] op_sel_hi:[0,1]
	v_pk_mul_f32 v[34:35], v[60:61], v[32:33] op_sel_hi:[0,1]
	v_pk_mul_f32 v[38:39], v[60:61], v[38:39] op_sel_hi:[0,1]
	v_pk_mul_f32 v[36:37], v[60:61], v[36:37] op_sel_hi:[0,1]
	v_cvt_pk_bf16_f32 v32, v36, v37
	v_cvt_pk_bf16_f32 v33, v38, v39
	v_cvt_pk_bf16_f32 v34, v34, v35
	v_cvt_pk_bf16_f32 v35, v40, v41
	global_store_dwordx4 v[48:49], v[32:35], off offset:256
.LBB0_1725:
	s_or_b64 exec, exec, s[30:31]
	s_nop 0
	v_add_u32_e32 v32, 0xa0, v147
	v_cmp_gt_i32_e32 vcc, s7, v32
	s_and_saveexec_b64 s[30:31], vcc
	s_cbranch_execz .LBB0_1727
	v_lshl_add_u32 v32, s52, 14, v32
	v_ashrrev_i32_e32 v33, 31, v32
	v_lshl_add_u64 v[32:33], v[32:33], 2, s[12:13]
	global_load_dword v40, v[32:33], off
	s_add_i32 s34, s52, s50
	s_ashr_i32 s35, s34, 31
	s_lshl_b64 s[34:35], s[34:35], 12
	s_add_u32 s34, s44, s34
	v_ashrrev_i32_e32 v143, 31, v142
	s_addc_u32 s35, s16, s35
	v_lshl_add_u64 v[42:43], v[142:143], 2, s[34:35]
	s_waitcnt vmcnt(0)
	v_ashrrev_i32_e32 v41, 31, v40
	v_lshl_add_u64 v[44:45], v[40:41], 2, s[14:15]
	global_load_dword v44, v[44:45], off
	v_lshlrev_b64 v[40:41], 11, v[40:41]
	v_lshl_add_u64 v[40:41], s[10:11], 0, v[40:41]
	v_pk_add_f32 v[30:31], v[30:31], v[166:167]
	v_pk_add_f32 v[26:27], v[26:27], v[170:171]
	v_pk_add_f32 v[24:25], v[24:25], v[168:169]
	v_pk_add_f32 v[28:29], v[28:29], v[164:165]
	v_lshl_add_u64 v[32:33], v[142:143], 1, v[40:41]
	s_waitcnt vmcnt(0)
	v_pk_mul_f32 v[34:35], v[44:45], v[26:27] op_sel_hi:[0,1]
	v_pk_mul_f32 v[26:27], v[44:45], v[24:25] op_sel_hi:[0,1]
	v_pk_mul_f32 v[30:31], v[44:45], v[30:31] op_sel_hi:[0,1]
	v_pk_mul_f32 v[28:29], v[44:45], v[28:29] op_sel_hi:[0,1]
	v_cvt_pk_bf16_f32 v24, v28, v29
	v_cvt_pk_bf16_f32 v25, v30, v31
	v_cvt_pk_bf16_f32 v26, v26, v27
	v_cvt_pk_bf16_f32 v27, v34, v35
	global_store_dwordx4 v[32:33], v[24:27], off
	v_pk_add_f32 v[22:23], v[22:23], v[174:175]
	v_pk_add_f32 v[18:19], v[18:19], v[178:179]
	v_pk_add_f32 v[16:17], v[16:17], v[176:177]
	v_pk_add_f32 v[20:21], v[20:21], v[172:173]
	v_pk_mul_f32 v[24:25], v[44:45], v[18:19] op_sel_hi:[0,1]
	v_pk_mul_f32 v[18:19], v[44:45], v[16:17] op_sel_hi:[0,1]
	v_pk_mul_f32 v[22:23], v[44:45], v[22:23] op_sel_hi:[0,1]
	v_pk_mul_f32 v[20:21], v[44:45], v[20:21] op_sel_hi:[0,1]
	v_cvt_pk_bf16_f32 v16, v20, v21
	v_cvt_pk_bf16_f32 v17, v22, v23
	v_cvt_pk_bf16_f32 v18, v18, v19
	v_cvt_pk_bf16_f32 v19, v24, v25
	global_store_dwordx4 v[32:33], v[16:19], off offset:256
.LBB0_1727:
	s_or_b64 exec, exec, s[30:31]
	s_nop 0
	v_add_u32_e32 v16, 0xb0, v147
	v_cmp_gt_i32_e32 vcc, s7, v16
	s_and_saveexec_b64 s[30:31], vcc
	s_cbranch_execz .LBB0_1729
	v_lshl_add_u32 v16, s52, 14, v16
	v_ashrrev_i32_e32 v17, 31, v16
	v_lshl_add_u64 v[16:17], v[16:17], 2, s[12:13]
	global_load_dword v24, v[16:17], off
	s_add_i32 s34, s52, s50
	s_ashr_i32 s35, s34, 31
	s_lshl_b64 s[34:35], s[34:35], 12
	s_add_u32 s34, s44, s34
	v_ashrrev_i32_e32 v143, 31, v142
	s_addc_u32 s35, s16, s35
	v_lshl_add_u64 v[26:27], v[142:143], 2, s[34:35]
	s_waitcnt vmcnt(0)
	v_ashrrev_i32_e32 v25, 31, v24
	v_lshl_add_u64 v[28:29], v[24:25], 2, s[14:15]
	global_load_dword v28, v[28:29], off
	v_lshlrev_b64 v[24:25], 11, v[24:25]
	v_lshl_add_u64 v[24:25], s[10:11], 0, v[24:25]
	v_pk_add_f32 v[14:15], v[14:15], v[166:167]
	v_pk_add_f32 v[10:11], v[10:11], v[170:171]
	v_pk_add_f32 v[8:9], v[8:9], v[168:169]
	v_pk_add_f32 v[12:13], v[12:13], v[164:165]
	v_lshl_add_u64 v[16:17], v[142:143], 1, v[24:25]
	s_waitcnt vmcnt(0)
	v_pk_mul_f32 v[18:19], v[28:29], v[10:11] op_sel_hi:[0,1]
	v_pk_mul_f32 v[10:11], v[28:29], v[8:9] op_sel_hi:[0,1]
	v_pk_mul_f32 v[14:15], v[28:29], v[14:15] op_sel_hi:[0,1]
	v_pk_mul_f32 v[12:13], v[28:29], v[12:13] op_sel_hi:[0,1]
	v_cvt_pk_bf16_f32 v8, v12, v13
	v_cvt_pk_bf16_f32 v9, v14, v15
	v_cvt_pk_bf16_f32 v10, v10, v11
	v_cvt_pk_bf16_f32 v11, v18, v19
	global_store_dwordx4 v[16:17], v[8:11], off
	v_pk_add_f32 v[6:7], v[6:7], v[174:175]
	v_pk_add_f32 v[2:3], v[2:3], v[178:179]
	v_pk_add_f32 v[0:1], v[0:1], v[176:177]
	v_pk_add_f32 v[4:5], v[4:5], v[172:173]
	v_pk_mul_f32 v[8:9], v[28:29], v[2:3] op_sel_hi:[0,1]
	v_pk_mul_f32 v[2:3], v[28:29], v[0:1] op_sel_hi:[0,1]
	v_pk_mul_f32 v[6:7], v[28:29], v[6:7] op_sel_hi:[0,1]
	v_pk_mul_f32 v[4:5], v[28:29], v[4:5] op_sel_hi:[0,1]
	v_cvt_pk_bf16_f32 v0, v4, v5
	v_cvt_pk_bf16_f32 v1, v6, v7
	v_cvt_pk_bf16_f32 v2, v2, v3
	v_cvt_pk_bf16_f32 v3, v8, v9
	global_store_dwordx4 v[16:17], v[0:3], off offset:256
